# combined counted-wait edits: XCD leader no ack wait + route loop vmcnt(2) + ln2 second-row POS loads hoisted, on top of mixer rewrite + flat release
# speedup vs baseline: 1.0041x; 1.0041x over previous
.LBB0_1020:
	s_add_i32 s0, s91, s49
	s_add_i32 s0, s0, s40
	s_add_i32 s40, s0, 8
	s_ashr_i32 s41, s40, 31
	s_lshl_b64 s[40:41], s[40:41], 10
	s_add_u32 s38, s38, s40
	s_addc_u32 s39, s39, s41
	s_ashr_i32 s1, s0, 31
	s_lshl_b64 s[0:1], s[0:1], 5
	v_and_b32_e32 v7, 56, v18
	s_add_u32 s0, s86, s0
	v_cmp_eq_u32_e64 s[18:19], 56, v7
	v_mov_b32_e32 v7, v69
	s_addc_u32 s1, s87, s1
	v_lshl_add_u64 v[14:15], s[38:39], 0, v[6:7]
	v_lshl_add_u64 v[6:7], s[0:1], 0, v[68:69]
	s_mov_b64 s[0:1], 0x359d4000
	v_cmp_gt_u32_e64 s[4:5], 8, v20
	v_cmp_lt_u32_e64 s[6:7], 7, v20
	v_cmp_lt_u32_e64 s[8:9], 15, v20
	v_cmp_lt_u32_e64 s[10:11], 23, v20
	v_cmp_lt_u32_e64 s[12:13], 31, v20
	v_cmp_lt_u32_e64 s[14:15], 39, v20
	v_cmp_lt_u32_e64 s[16:17], 47, v20
	v_cmp_eq_u32_e64 s[20:21], 0, v20
	v_cmp_eq_u32_e64 s[22:23], 1, v20
	v_cmp_eq_u32_e64 s[24:25], 2, v20
	v_cmp_eq_u32_e64 s[26:27], 3, v20
	v_cmp_eq_u32_e64 s[28:29], 4, v20
	v_cmp_eq_u32_e64 s[30:31], 5, v20
	v_cmp_eq_u32_e64 s[34:35], 6, v20
	v_cmp_eq_u32_e64 s[36:37], 7, v20
	v_lshl_add_u64 v[16:17], v[6:7], 0, s[0:1]
	s_waitcnt vmcnt(0)
	s_branch .LBB0_1023

.LBB0_1022:
	s_waitcnt vmcnt(2)
	v_mov_b64_e32 v[12:13], v[8:9]
	s_and_b64 vcc, exec, s[74:75]
	v_mov_b64_e32 v[10:11], v[6:7]
	s_cbranch_vccnz .LBB0_1106
.LBB0_1023:
	s_add_i32 s0, s51, s49
	s_cmp_gt_i32 s0, 0x83ff
	s_mov_b64 s[74:75], -1
	s_cbranch_scc1 .LBB0_1022
	s_add_i32 s49, s49, 8
	s_cmp_ge_i32 s49, s50
	s_cselect_b64 s[74:75], -1, 0
	s_cmp_gt_i32 s0, 0x83f7
	s_cselect_b64 s[0:1], -1, 0
	s_or_b64 s[0:1], s[74:75], s[0:1]
	s_waitcnt vmcnt(2)
	v_mov_b64_e32 v[6:7], v[10:11]
	s_and_b64 vcc, exec, s[0:1]
	v_mov_b64_e32 v[8:9], v[12:13]
	s_cbranch_vccnz .LBB0_1026
	global_load_dwordx4 v[6:9], v[14:15], off

.LBB0_1675:
	s_add_i32 s5, s34, s4
	s_cmp_lt_i32 s5, 0x8400
	s_cselect_b32 s0, s5, s4
	s_ashr_i32 s1, s0, 31
	s_lshl_b64 s[16:17], s[0:1], 5
	s_add_u32 s18, s28, s16
	s_addc_u32 s19, s29, s17
	global_load_dwordx4 v[38:41], v69, s[18:19] offset:16
	global_load_dwordx4 v[42:45], v69, s[18:19]
	s_add_u32 s16, s30, s16
	s_addc_u32 s17, s31, s17
	global_load_dwordx4 v[34:37], v69, s[16:17] offset:16
	global_load_dwordx4 v[46:49], v69, s[16:17]
	s_add_u32 s48, s2, s12
	s_addc_u32 s49, s3, s13
	s_add_u32 s48, s48, 0x35adc000
	s_addc_u32 s49, s49, 0
	global_load_dwordx4 v[126:129], v69, s[48:49]
	global_load_dwordx4 v[130:133], v69, s[48:49] offset:16
	s_lshl_b64 s[16:17], s[0:1], 10
	s_mov_b32 s7, 0x14800000
	s_lshl_b64 s[18:19], s[0:1], 11
	v_lshl_add_u64 v[90:91], s[2:3], 0, v[156:157]
	s_mov_b64 s[0:1], 0x1cccc000
	v_lshl_add_u64 v[94:95], v[90:91], 0, s[0:1]
	s_mov_b32 s0, 0x1cccc000
	v_readlane_b32 s38, v247, 34
	v_readlane_b32 s39, v247, 35
	s_waitcnt vmcnt(4)
	v_ashrrev_i32_e32 v51, 31, v42
	v_mov_b32_e32 v50, v42
	v_lshlrev_b64 v[50:51], 10, v[50:51]
	v_lshl_add_u64 v[50:51], v[144:145], 0, v[50:51]
	global_load_dwordx4 v[82:85], v[50:51], off nt
	v_ashrrev_i32_e32 v51, 31, v43
	v_mov_b32_e32 v50, v43
	v_lshlrev_b64 v[42:43], 10, v[50:51]
	v_lshl_add_u64 v[42:43], v[144:145], 0, v[42:43]
	global_load_dwordx4 v[78:81], v[42:43], off nt
	v_ashrrev_i32_e32 v43, 31, v44
	v_mov_b32_e32 v42, v44
	v_lshlrev_b64 v[42:43], 10, v[42:43]
	v_lshl_add_u64 v[42:43], v[144:145], 0, v[42:43]
	global_load_dwordx4 v[74:77], v[42:43], off nt
	v_ashrrev_i32_e32 v43, 31, v45
	v_mov_b32_e32 v42, v45
	v_lshlrev_b64 v[42:43], 10, v[42:43]
	v_lshl_add_u64 v[42:43], v[144:145], 0, v[42:43]
	global_load_dwordx4 v[70:73], v[42:43], off nt
	v_ashrrev_i32_e32 v43, 31, v38
	v_mov_b32_e32 v42, v38
	v_lshlrev_b64 v[42:43], 10, v[42:43]
	v_lshl_add_u64 v[42:43], v[144:145], 0, v[42:43]
	global_load_dwordx4 v[62:65], v[42:43], off nt
	v_ashrrev_i32_e32 v43, 31, v39
	v_mov_b32_e32 v42, v39
	v_lshlrev_b64 v[38:39], 10, v[42:43]
	v_lshl_add_u64 v[38:39], v[144:145], 0, v[38:39]
	global_load_dwordx4 v[58:61], v[38:39], off nt
	v_ashrrev_i32_e32 v39, 31, v40
	v_mov_b32_e32 v38, v40
	v_lshlrev_b64 v[38:39], 10, v[38:39]
	v_lshl_add_u64 v[38:39], v[144:145], 0, v[38:39]
	global_load_dwordx4 v[54:57], v[38:39], off nt
	v_ashrrev_i32_e32 v39, 31, v41
	v_mov_b32_e32 v38, v41
	v_lshlrev_b64 v[38:39], 10, v[38:39]
	v_lshl_add_u64 v[38:39], v[144:145], 0, v[38:39]
	global_load_dwordx4 v[50:53], v[38:39], off nt
	v_lshl_add_u64 v[38:39], v[144:145], 0, s[16:17]
	v_add_co_u32_e32 v38, vcc, s7, v38
	s_nop 1
	v_addc_co_u32_e32 v39, vcc, 0, v39, vcc
	v_add_co_u32_e32 v90, vcc, s0, v90
	s_add_i32 s0, s4, 0x52000
	s_ashr_i32 s1, s0, 31
	s_lshl_b64 s[0:1], s[0:1], 10
	v_lshl_add_u64 v[98:99], v[144:145], 0, s[0:1]
	s_add_u32 s0, s2, s12
	s_addc_u32 s1, s3, s13
	global_load_dwordx4 v[86:89], v[38:39], off nt
	v_lshl_add_u64 v[38:39], v[146:147], 0, s[18:19]
	v_addc_co_u32_e32 v91, vcc, 0, v91, vcc
	s_add_u32 s20, s0, 0x35adc000
	global_load_dwordx4 v[42:45], v[38:39], off offset:16
	s_nop 0
	global_load_dwordx4 v[38:41], v[38:39], off
	s_nop 0
	global_load_dwordx4 v[90:93], v[90:91], off
	s_nop 0
	global_load_dwordx4 v[94:97], v[94:95], off offset:16
	s_addc_u32 s21, s1, 0
	global_load_dwordx4 v[102:105], v[98:99], off nt
	s_nop 0
	s_waitcnt vmcnt(14)
	v_mov_b32_e32 v98, v126
	v_mov_b32_e32 v99, v127
	v_mov_b32_e32 v100, v128
	v_mov_b32_e32 v101, v129
	v_mov_b32_e32 v118, v130
	v_mov_b32_e32 v119, v131
	v_mov_b32_e32 v120, v132
	v_mov_b32_e32 v121, v133
	s_add_u32 s20, s0, 0x359d4000
	s_addc_u32 s21, s1, 0
	v_ashrrev_i32_e32 v107, 31, v121
	v_mov_b32_e32 v106, v121
	v_ashrrev_i32_e32 v123, 31, v101
	v_mov_b32_e32 v122, v101
	v_ashrrev_i32_e32 v101, 31, v100
	v_lshlrev_b64 v[106:107], 10, v[106:107]
	v_lshlrev_b64 v[100:101], 10, v[100:101]
	v_lshl_add_u64 v[106:107], v[144:145], 0, v[106:107]
	v_lshl_add_u64 v[100:101], v[144:145], 0, v[100:101]
	global_load_dwordx4 v[106:109], v[106:107], off nt
	v_ashrrev_i32_e32 v121, 31, v120
	global_load_dwordx4 v[126:129], v[100:101], off nt
	v_ashrrev_i32_e32 v101, 31, v99
	v_mov_b32_e32 v100, v99
	v_ashrrev_i32_e32 v99, 31, v98
	v_lshlrev_b64 v[100:101], 10, v[100:101]
	v_lshlrev_b64 v[98:99], 10, v[98:99]
	v_lshl_add_u64 v[100:101], v[144:145], 0, v[100:101]
	v_lshl_add_u64 v[98:99], v[144:145], 0, v[98:99]
	global_load_dwordx4 v[130:133], v[100:101], off nt
	global_load_dwordx4 v[134:137], v[98:99], off nt
	v_ashrrev_i32_e32 v115, 31, v119
	v_mov_b32_e32 v114, v119
	v_ashrrev_i32_e32 v119, 31, v118
	v_lshlrev_b64 v[110:111], 10, v[120:121]
	v_lshlrev_b64 v[114:115], 10, v[114:115]
	v_lshlrev_b64 v[118:119], 10, v[118:119]
	v_lshlrev_b64 v[122:123], 10, v[122:123]
	v_lshl_add_u64 v[110:111], v[144:145], 0, v[110:111]
	v_lshl_add_u64 v[114:115], v[144:145], 0, v[114:115]
	v_lshl_add_u64 v[118:119], v[144:145], 0, v[118:119]
	v_lshl_add_u64 v[122:123], v[144:145], 0, v[122:123]
	global_load_dwordx4 v[110:113], v[110:111], off nt
	global_load_dwordx4 v[114:117], v[114:115], off nt
	global_load_dwordx4 v[118:121], v[118:119], off nt
	global_load_dwordx4 v[122:125], v[122:123], off nt
	s_nop 0
	global_load_dwordx4 v[98:101], v69, s[20:21] offset:16
	global_load_dwordx4 v[138:141], v239, s[0:1]
	s_waitcnt vmcnt(8)
	v_cvt_pk_f32_fp8_sdwa v[218:219], v104 src0_sel:WORD_1
	v_cvt_pk_f32_fp8_e32 v[224:225], v105
	v_cvt_pk_f32_fp8_sdwa v[230:231], v105 src0_sel:WORD_1
	v_cvt_pk_f32_fp8_sdwa v[212:213], v108 src0_sel:WORD_1
	v_cvt_pk_f32_fp8_sdwa v[184:185], v126 src0_sel:WORD_1
	v_cvt_pk_f32_fp8_e32 v[186:187], v127
	v_cvt_pk_f32_fp8_e32 v[188:189], v128
	v_cvt_pk_f32_fp8_sdwa v[190:191], v128 src0_sel:WORD_1
	v_cvt_pk_f32_fp8_e32 v[192:193], v129
	v_cvt_pk_f32_fp8_sdwa v[194:195], v129 src0_sel:WORD_1
	s_add_i32 s20, s4, 0xfffffc00
	s_waitcnt vmcnt(7)
	v_cvt_pk_f32_fp8_e32 v[170:171], v130
	s_waitcnt vmcnt(6)
	v_cvt_pk_f32_fp8_e32 v[158:159], v134
	v_cvt_pk_f32_fp8_sdwa v[160:161], v134 src0_sel:WORD_1
	v_cvt_pk_f32_fp8_e32 v[162:163], v135
	v_cvt_pk_f32_fp8_sdwa v[134:135], v135 src0_sel:WORD_1
	v_cvt_pk_f32_fp8_e32 v[176:177], v132
	v_cvt_pk_f32_fp8_sdwa v[178:179], v132 src0_sel:WORD_1
	v_cvt_pk_f32_fp8_e32 v[180:181], v133
	v_cvt_pk_f32_fp8_sdwa v[182:183], v133 src0_sel:WORD_1
	v_cvt_pk_f32_fp8_e32 v[132:133], v126
	v_cvt_pk_f32_fp8_sdwa v[172:173], v130 src0_sel:WORD_1
	v_cvt_pk_f32_fp8_e32 v[174:175], v131
	v_cvt_pk_f32_fp8_sdwa v[130:131], v131 src0_sel:WORD_1
	v_cvt_pk_f32_fp8_sdwa v[126:127], v127 src0_sel:WORD_1
	v_cvt_pk_f32_fp8_e32 v[164:165], v136
	v_cvt_pk_f32_fp8_sdwa v[166:167], v136 src0_sel:WORD_1
	v_cvt_pk_f32_fp8_e32 v[168:169], v137
	v_cvt_pk_f32_fp8_sdwa v[136:137], v137 src0_sel:WORD_1
	s_lshr_b32 s0, s20, 13
	s_mulk_i32 s0, 0x1800
	s_cmpk_gt_i32 s4, 0x3ff
	s_cselect_b32 s66, s0, 0x6000
	s_lshl_b64 s[22:23], s[66:67], 2
	s_add_u32 s0, s24, s22
	s_addc_u32 s1, s25, s23
	s_waitcnt vmcnt(3)
	v_cvt_pk_f32_fp8_sdwa v[216:217], v121 src0_sel:WORD_1
	v_cvt_pk_f32_fp8_sdwa v[222:223], v117 src0_sel:WORD_1
	v_cvt_pk_f32_fp8_e32 v[214:215], v113
	v_cvt_pk_f32_fp8_sdwa v[226:227], v113 src0_sel:WORD_1
	v_cvt_pk_f32_fp8_e32 v[220:221], v109
	v_cvt_pk_f32_fp8_sdwa v[228:229], v109 src0_sel:WORD_1
	s_waitcnt vmcnt(2)
	v_cvt_pk_f32_fp8_e32 v[128:129], v122
	v_cvt_pk_f32_fp8_sdwa v[196:197], v122 src0_sel:WORD_1
	v_cvt_pk_f32_fp8_e32 v[200:201], v123
	v_cvt_pk_f32_fp8_sdwa v[202:203], v123 src0_sel:WORD_1
	s_waitcnt vmcnt(0)
	v_pk_fma_f32 v[122:123], v[138:139], v[158:159], 0 op_sel_hi:[0,1,0]
	v_pk_fma_f32 v[122:123], v[138:139], v[170:171], v[122:123] op_sel:[1,0,0]
	v_cvt_pk_f32_fp8_e32 v[204:205], v124
	v_pk_fma_f32 v[122:123], v[140:141], v[132:133], v[122:123] op_sel_hi:[0,1,1]
	v_pk_fma_f32 v[132:133], v[138:139], v[134:135], 0 op_sel_hi:[0,1,0]
	v_pk_fma_f32 v[130:131], v[138:139], v[130:131], v[132:133] op_sel:[1,0,0]
	v_mov_b32_e32 v158, v141
	v_pk_fma_f32 v[126:127], v[140:141], v[126:127], v[130:131] op_sel_hi:[0,1,1]
	v_pk_fma_f32 v[132:133], v[158:159], v[202:203], v[126:127] op_sel_hi:[0,1,1]
	v_pk_fma_f32 v[126:127], v[138:139], v[164:165], 0 op_sel_hi:[0,1,0]
	v_pk_fma_f32 v[126:127], v[138:139], v[176:177], v[126:127] op_sel:[1,0,0]
	v_cvt_pk_f32_fp8_sdwa v[206:207], v124 src0_sel:WORD_1
	v_pk_fma_f32 v[126:127], v[140:141], v[188:189], v[126:127] op_sel_hi:[0,1,1]
	v_pk_fma_f32 v[122:123], v[158:159], v[128:129], v[122:123] op_sel_hi:[0,1,1]
	v_pk_fma_f32 v[128:129], v[138:139], v[162:163], 0 op_sel_hi:[0,1,0]
	v_pk_fma_f32 v[162:163], v[158:159], v[204:205], v[126:127] op_sel_hi:[0,1,1]
	v_pk_fma_f32 v[126:127], v[138:139], v[166:167], 0 op_sel_hi:[0,1,0]
	v_pk_fma_f32 v[126:127], v[138:139], v[178:179], v[126:127] op_sel:[1,0,0]
	v_cvt_pk_f32_fp8_e32 v[208:209], v125
	v_pk_fma_f32 v[126:127], v[140:141], v[190:191], v[126:127] op_sel_hi:[0,1,1]
	v_pk_fma_f32 v[176:177], v[158:159], v[206:207], v[126:127] op_sel_hi:[0,1,1]
	v_pk_fma_f32 v[126:127], v[138:139], v[168:169], 0 op_sel_hi:[0,1,0]
	v_pk_fma_f32 v[126:127], v[138:139], v[180:181], v[126:127] op_sel:[1,0,0]
	v_cvt_pk_f32_fp8_sdwa v[210:211], v125 src0_sel:WORD_1
	v_pk_fma_f32 v[126:127], v[140:141], v[192:193], v[126:127] op_sel_hi:[0,1,1]
	v_pk_fma_f32 v[124:125], v[138:139], v[160:161], 0 op_sel_hi:[0,1,0]
	v_pk_fma_f32 v[192:193], v[158:159], v[208:209], v[126:127] op_sel_hi:[0,1,1]
	v_pk_fma_f32 v[126:127], v[138:139], v[136:137], 0 op_sel_hi:[0,1,0]
	v_pk_fma_f32 v[124:125], v[138:139], v[172:173], v[124:125] op_sel:[1,0,0]
	v_pk_fma_f32 v[128:129], v[138:139], v[174:175], v[128:129] op_sel:[1,0,0]
	v_pk_fma_f32 v[126:127], v[138:139], v[182:183], v[126:127] op_sel:[1,0,0]
	v_pk_fma_f32 v[124:125], v[140:141], v[184:185], v[124:125] op_sel_hi:[0,1,1]
	v_pk_fma_f32 v[128:129], v[140:141], v[186:187], v[128:129] op_sel_hi:[0,1,1]
	v_pk_fma_f32 v[126:127], v[140:141], v[194:195], v[126:127] op_sel_hi:[0,1,1]
	v_pk_fma_f32 v[124:125], v[158:159], v[196:197], v[124:125] op_sel_hi:[0,1,1]
	v_pk_fma_f32 v[128:129], v[158:159], v[200:201], v[128:129] op_sel_hi:[0,1,1]
	v_pk_fma_f32 v[210:211], v[158:159], v[210:211], v[126:127] op_sel_hi:[0,1,1]
	v_cvt_pk_f32_fp8_e32 v[158:159], v102
	v_cvt_pk_f32_fp8_sdwa v[170:171], v102 src0_sel:WORD_1
	v_cvt_pk_f32_fp8_e32 v[182:183], v103
	v_cvt_pk_f32_fp8_sdwa v[194:195], v103 src0_sel:WORD_1
	v_lshl_add_u64 v[102:103], s[0:1], 0, v[68:69]
	s_mov_b64 s[0:1], 0x15000
	v_cvt_pk_f32_fp8_e32 v[126:127], v118
	v_cvt_pk_f32_fp8_sdwa v[130:131], v118 src0_sel:WORD_1
	v_cvt_pk_f32_fp8_e32 v[138:139], v119
	v_cvt_pk_f32_fp8_sdwa v[166:167], v119 src0_sel:WORD_1
	v_cvt_pk_f32_fp8_e32 v[118:119], v114
	v_cvt_pk_f32_fp8_sdwa v[134:135], v114 src0_sel:WORD_1
	v_cvt_pk_f32_fp8_e32 v[160:161], v115
	v_cvt_pk_f32_fp8_sdwa v[172:173], v115 src0_sel:WORD_1
	v_lshl_add_u64 v[114:115], v[102:103], 0, s[0:1]
	v_add_co_u32_e32 v102, vcc, s36, v102
	v_cvt_pk_f32_fp8_e32 v[178:179], v120
	s_nop 0
	v_addc_co_u32_e32 v103, vcc, 0, v103, vcc
	v_cvt_pk_f32_fp8_sdwa v[188:189], v120 src0_sel:WORD_1
	v_cvt_pk_f32_fp8_e32 v[202:203], v121
	v_cvt_pk_f32_fp8_e32 v[184:185], v116
	v_cvt_pk_f32_fp8_sdwa v[196:197], v116 src0_sel:WORD_1
	v_cvt_pk_f32_fp8_e32 v[208:209], v117
	v_cvt_pk_f32_fp8_e32 v[120:121], v110
	v_cvt_pk_f32_fp8_sdwa v[140:141], v110 src0_sel:WORD_1
	v_cvt_pk_f32_fp8_e32 v[168:169], v111
	v_cvt_pk_f32_fp8_sdwa v[180:181], v111 src0_sel:WORD_1
	v_cvt_pk_f32_fp8_e32 v[190:191], v112
	v_cvt_pk_f32_fp8_sdwa v[204:205], v112 src0_sel:WORD_1
	v_cvt_pk_f32_fp8_e32 v[136:137], v106
	v_cvt_pk_f32_fp8_sdwa v[164:165], v106 src0_sel:WORD_1
	v_cvt_pk_f32_fp8_e32 v[174:175], v107
	v_cvt_pk_f32_fp8_sdwa v[186:187], v107 src0_sel:WORD_1
	v_cvt_pk_f32_fp8_e32 v[200:201], v108
	v_cvt_pk_f32_fp8_e32 v[206:207], v104
	global_load_dwordx4 v[102:105], v[102:103], off
	s_nop 0
	global_load_dwordx4 v[106:109], v[114:115], off offset:16
	global_load_dwordx4 v[110:113], v[114:115], off offset:32
	s_nop 0
	global_load_dwordx4 v[114:117], v[114:115], off offset:48
	v_pk_fma_f32 v[192:193], v[98:99], v[202:203], v[192:193] op_sel_hi:[0,1,1]
	v_pk_fma_f32 v[192:193], v[98:99], v[208:209], v[192:193] op_sel:[1,0,0]
	v_pk_fma_f32 v[210:211], v[98:99], v[216:217], v[210:211] op_sel_hi:[0,1,1]
	v_mov_b32_e32 v216, v101
	v_pk_fma_f32 v[192:193], v[100:101], v[214:215], v[192:193] op_sel_hi:[0,1,1]
	v_pk_fma_f32 v[192:193], v[216:217], v[220:221], v[192:193] op_sel_hi:[0,1,1]
	v_pk_add_f32 v[192:193], v[192:193], v[224:225]
	v_pk_fma_f32 v[210:211], v[98:99], v[222:223], v[210:211] op_sel:[1,0,0]
	v_lshlrev_b32_e32 v222, 16, v97
	v_and_b32_e32 v223, 0xffff0000, v97
	v_lshlrev_b32_e32 v202, 16, v96
	v_and_b32_e32 v203, 0xffff0000, v96
	v_pk_fma_f32 v[210:211], v[100:101], v[226:227], v[210:211] op_sel_hi:[0,1,1]
	v_pk_fma_f32 v[210:211], v[216:217], v[228:229], v[210:211] op_sel_hi:[0,1,1]
	v_pk_add_f32 v[210:211], v[210:211], v[230:231]
	s_waitcnt vmcnt(0)
	v_pk_mul_f32 v[96:97], v[192:193], v[114:115]
	v_pk_fma_f32 v[114:115], v[98:99], v[188:189], v[176:177] op_sel_hi:[0,1,1]
	v_pk_fma_f32 v[114:115], v[98:99], v[196:197], v[114:115] op_sel:[1,0,0]
	v_lshlrev_b32_e32 v176, 16, v95
	v_pk_fma_f32 v[114:115], v[100:101], v[204:205], v[114:115] op_sel_hi:[0,1,1]
	v_pk_fma_f32 v[114:115], v[216:217], v[212:213], v[114:115] op_sel_hi:[0,1,1]
	v_pk_add_f32 v[114:115], v[114:115], v[218:219]
	v_and_b32_e32 v177, 0xffff0000, v95
	v_pk_mul_f32 v[112:113], v[114:115], v[112:113]
	v_pk_fma_f32 v[114:115], v[98:99], v[178:179], v[162:163] op_sel_hi:[0,1,1]
	v_pk_fma_f32 v[114:115], v[98:99], v[184:185], v[114:115] op_sel:[1,0,0]
	v_lshlrev_b32_e32 v162, 16, v94
	v_pk_fma_f32 v[114:115], v[100:101], v[190:191], v[114:115] op_sel_hi:[0,1,1]
	v_pk_fma_f32 v[114:115], v[216:217], v[200:201], v[114:115] op_sel_hi:[0,1,1]
	v_pk_add_f32 v[114:115], v[114:115], v[206:207]
	v_and_b32_e32 v163, 0xffff0000, v94
	v_pk_mul_f32 v[94:95], v[114:115], v[110:111]
	v_pk_fma_f32 v[110:111], v[98:99], v[166:167], v[132:133] op_sel_hi:[0,1,1]
	v_pk_fma_f32 v[110:111], v[98:99], v[172:173], v[110:111] op_sel:[1,0,0]
	v_lshlrev_b32_e32 v114, 16, v93
	v_pk_fma_f32 v[110:111], v[100:101], v[180:181], v[110:111] op_sel_hi:[0,1,1]
	v_pk_fma_f32 v[110:111], v[216:217], v[186:187], v[110:111] op_sel_hi:[0,1,1]
	v_pk_add_f32 v[110:111], v[110:111], v[194:195]
	v_and_b32_e32 v115, 0xffff0000, v93
	v_pk_mul_f32 v[108:109], v[110:111], v[108:109]
	v_pk_fma_f32 v[110:111], v[98:99], v[138:139], v[128:129] op_sel_hi:[0,1,1]
	v_pk_fma_f32 v[110:111], v[98:99], v[160:161], v[110:111] op_sel:[1,0,0]
	v_pk_fma_f32 v[108:109], v[114:115], s[82:83], v[108:109] op_sel_hi:[1,0,1]
	v_pk_fma_f32 v[110:111], v[100:101], v[168:169], v[110:111] op_sel_hi:[0,1,1]
	v_pk_fma_f32 v[110:111], v[216:217], v[174:175], v[110:111] op_sel_hi:[0,1,1]
	v_pk_add_f32 v[110:111], v[110:111], v[182:183]
	v_lshlrev_b32_e32 v114, 16, v92
	v_and_b32_e32 v115, 0xffff0000, v92
	v_pk_mul_f32 v[92:93], v[110:111], v[106:107]
	v_pk_fma_f32 v[106:107], v[98:99], v[130:131], v[124:125] op_sel_hi:[0,1,1]
	v_pk_fma_f32 v[106:107], v[98:99], v[134:135], v[106:107] op_sel:[1,0,0]
	v_lshlrev_b32_e32 v110, 16, v91
	v_pk_fma_f32 v[106:107], v[100:101], v[140:141], v[106:107] op_sel_hi:[0,1,1]
	v_pk_fma_f32 v[106:107], v[216:217], v[164:165], v[106:107] op_sel_hi:[0,1,1]
	v_pk_add_f32 v[106:107], v[106:107], v[170:171]
	v_and_b32_e32 v111, 0xffff0000, v91
	v_pk_mul_f32 v[104:105], v[106:107], v[104:105]
	v_pk_fma_f32 v[106:107], v[98:99], v[126:127], v[122:123] op_sel_hi:[0,1,1]
	v_pk_fma_f32 v[98:99], v[98:99], v[118:119], v[106:107] op_sel:[1,0,0]
	v_pk_fma_f32 v[104:105], v[110:111], s[82:83], v[104:105] op_sel_hi:[1,0,1]
	v_pk_fma_f32 v[98:99], v[100:101], v[120:121], v[98:99] op_sel_hi:[0,1,1]
	v_pk_fma_f32 v[98:99], v[216:217], v[136:137], v[98:99] op_sel_hi:[0,1,1]
	v_pk_add_f32 v[98:99], v[98:99], v[158:159]
	v_lshlrev_b32_e32 v100, 16, v90
	v_and_b32_e32 v101, 0xffff0000, v90
	v_pk_mul_f32 v[90:91], v[98:99], v[102:103]
	v_pk_fma_f32 v[92:93], v[114:115], s[82:83], v[92:93] op_sel_hi:[1,0,1]
	v_pk_fma_f32 v[90:91], v[100:101], s[82:83], v[90:91] op_sel_hi:[1,0,1]
	v_pk_fma_f32 v[94:95], v[162:163], s[82:83], v[94:95] op_sel_hi:[1,0,1]
	v_add_f32_e32 v98, 0, v90
	v_add_f32_e32 v98, v91, v98
	v_add_f32_e32 v98, v104, v98
	v_add_f32_e32 v98, v105, v98
	v_add_f32_e32 v98, v92, v98
	v_add_f32_e32 v98, v93, v98
	v_add_f32_e32 v98, v108, v98
	v_add_f32_e32 v98, v109, v98
	v_add_f32_e32 v98, v94, v98
	v_pk_fma_f32 v[112:113], v[176:177], s[82:83], v[112:113] op_sel_hi:[1,0,1]
	v_add_f32_e32 v98, v95, v98
	v_add_f32_e32 v98, v112, v98
	v_pk_fma_f32 v[96:97], v[202:203], s[82:83], v[96:97] op_sel_hi:[1,0,1]
	v_add_f32_e32 v98, v113, v98
	v_pk_mul_f32 v[116:117], v[210:211], v[116:117]
	v_add_f32_e32 v98, v96, v98
	v_pk_fma_f32 v[116:117], v[222:223], s[82:83], v[116:117] op_sel_hi:[1,0,1]
	v_add_f32_e32 v98, v97, v98
	v_add_f32_e32 v98, v116, v98
	v_add_f32_e32 v98, v117, v98
	v_add_u32_e32 v178, s35, v142
	s_nop 0
	v_add_f32_dpp v98, v98, v98 quad_perm:[1,0,3,2] row_mask:0xf bank_mask:0xf bound_ctrl:1
	s_nop 1
	v_add_f32_dpp v98, v98, v98 quad_perm:[2,3,0,1] row_mask:0xf bank_mask:0xf bound_ctrl:1
	s_nop 1
	v_add_f32_dpp v98, v98, v98 row_half_mirror row_mask:0xf bank_mask:0xf bound_ctrl:1
	s_nop 1
	v_add_f32_dpp v98, v98, v98 row_mirror row_mask:0xf bank_mask:0xf bound_ctrl:1
	s_nop 0
	v_readlane_b32 s7, v98, 16
	v_readlane_b32 s21, v98, 48
	v_readlane_b32 s0, v98, 0
	v_readlane_b32 s1, v98, 32
	v_mov_b32_e32 v98, s7
	v_mov_b32_e32 v99, s21
	v_pk_add_f32 v[98:99], s[0:1], v[98:99]
	s_nop 0
	v_add_f32_e32 v98, v98, v99
	v_mul_f32_e32 v98, 0x3a800000, v98
	v_pk_add_f32 v[90:91], v[90:91], v[98:99] op_sel_hi:[1,0] neg_lo:[0,1] neg_hi:[0,1]
	v_pk_add_f32 v[104:105], v[104:105], v[98:99] op_sel_hi:[1,0] neg_lo:[0,1] neg_hi:[0,1]
	v_pk_mul_f32 v[100:101], v[90:91], v[90:91]
	v_pk_mul_f32 v[102:103], v[104:105], v[104:105]
	v_add_f32_e32 v100, v100, v101
	v_pk_add_f32 v[92:93], v[92:93], v[98:99] op_sel_hi:[1,0] neg_lo:[0,1] neg_hi:[0,1]
	v_add_f32_e32 v100, v102, v100
	v_pk_mul_f32 v[106:107], v[92:93], v[92:93]
	v_add_f32_e32 v100, v103, v100
	v_pk_add_f32 v[108:109], v[108:109], v[98:99] op_sel_hi:[1,0] neg_lo:[0,1] neg_hi:[0,1]
	v_add_f32_e32 v100, v106, v100
	v_pk_mul_f32 v[110:111], v[108:109], v[108:109]
	v_add_f32_e32 v100, v107, v100
	v_pk_add_f32 v[94:95], v[94:95], v[98:99] op_sel_hi:[1,0] neg_lo:[0,1] neg_hi:[0,1]
	v_add_f32_e32 v100, v110, v100
	v_pk_mul_f32 v[114:115], v[94:95], v[94:95]
	v_add_f32_e32 v100, v111, v100
	v_pk_add_f32 v[112:113], v[112:113], v[98:99] op_sel_hi:[1,0] neg_lo:[0,1] neg_hi:[0,1]
	v_add_f32_e32 v100, v114, v100
	v_pk_mul_f32 v[118:119], v[112:113], v[112:113]
	v_add_f32_e32 v100, v115, v100
	v_pk_add_f32 v[120:121], v[96:97], v[98:99] op_sel_hi:[1,0] neg_lo:[0,1] neg_hi:[0,1]
	v_add_f32_e32 v100, v118, v100
	v_pk_mul_f32 v[96:97], v[120:121], v[120:121]
	v_add_f32_e32 v100, v119, v100
	v_pk_add_f32 v[116:117], v[116:117], v[98:99] op_sel_hi:[1,0] neg_lo:[0,1] neg_hi:[0,1]
	v_add_f32_e32 v96, v96, v100
	v_pk_mul_f32 v[98:99], v[116:117], v[116:117]
	v_add_f32_e32 v96, v97, v96
	v_add_f32_e32 v96, v98, v96
	v_add_f32_e32 v96, v99, v96
	s_nop 1
	v_add_f32_dpp v96, v96, v96 quad_perm:[1,0,3,2] row_mask:0xf bank_mask:0xf bound_ctrl:1
	s_nop 1
	v_add_f32_dpp v96, v96, v96 quad_perm:[2,3,0,1] row_mask:0xf bank_mask:0xf bound_ctrl:1
	s_nop 1
	v_add_f32_dpp v96, v96, v96 row_half_mirror row_mask:0xf bank_mask:0xf bound_ctrl:1
	s_nop 1
	v_add_f32_dpp v96, v96, v96 row_mirror row_mask:0xf bank_mask:0xf bound_ctrl:1
	s_nop 0
	v_readlane_b32 s7, v96, 16
	v_readlane_b32 s21, v96, 48
	v_readlane_b32 s0, v96, 0
	v_readlane_b32 s1, v96, 32
	v_mov_b32_e32 v96, s7
	v_mov_b32_e32 v97, s21
	v_pk_add_f32 v[96:97], s[0:1], v[96:97]
	s_mov_b64 s[0:1], -1
	v_add_f32_e32 v96, v96, v97
	v_fmamk_f32 v96, v96, 0x3a800000, v236
	v_cmp_gt_f32_e32 vcc, s93, v96
	v_mul_f32_e32 v97, 0x4b800000, v96
	s_nop 0
	v_cndmask_b32_e32 v96, v96, v97, vcc
	v_rsq_f32_e32 v96, v96
	s_nop 0
	v_mul_f32_e32 v97, 0x45800000, v96
	v_cndmask_b32_e32 v100, v96, v97, vcc
	v_pk_mul_f32 v[90:91], v[90:91], v[100:101] op_sel_hi:[1,0]
	s_and_b64 vcc, exec, s[38:39]
	v_pk_fma_f32 v[102:103], v[14:15], v[90:91], v[18:19]
	v_pk_mul_f32 v[90:91], v[104:105], v[100:101] op_sel_hi:[1,0]
	s_nop 0
	v_pk_fma_f32 v[104:105], v[16:17], v[90:91], v[20:21]
	v_pk_mul_f32 v[90:91], v[92:93], v[100:101] op_sel_hi:[1,0]
	s_nop 0
	v_pk_fma_f32 v[106:107], v[10:11], v[90:91], v[22:23]
	v_pk_mul_f32 v[90:91], v[108:109], v[100:101] op_sel_hi:[1,0]
	s_nop 0
	v_pk_fma_f32 v[108:109], v[12:13], v[90:91], v[24:25]
	v_pk_mul_f32 v[90:91], v[94:95], v[100:101] op_sel_hi:[1,0]
	s_nop 0
	v_pk_fma_f32 v[94:95], v[6:7], v[90:91], v[26:27]
	v_pk_mul_f32 v[90:91], v[112:113], v[100:101] op_sel_hi:[1,0]
	s_nop 0
	v_pk_fma_f32 v[96:97], v[8:9], v[90:91], v[28:29]
	v_pk_mul_f32 v[90:91], v[120:121], v[100:101] op_sel_hi:[1,0]
	s_nop 0
	v_pk_fma_f32 v[98:99], v[2:3], v[90:91], v[30:31]
	v_pk_mul_f32 v[90:91], v[116:117], v[100:101] op_sel_hi:[1,0]
	s_nop 0
	v_pk_fma_f32 v[100:101], v[4:5], v[90:91], v[32:33]
	s_cbranch_vccnz .LBB0_1678
	s_andn2_b64 vcc, exec, s[0:1]
	s_cbranch_vccz .LBB0_1679
